# MLA masked-tile loop: short head, straight-line rescale test, pair-swap copies folded into converts, hoisted lane-swap index
# speedup vs baseline: 1.0245x; 1.0022x over previous
.LBB0_744:
	v_exp_f32_e32 v214, v16
	v_exp_f32_e32 v216, v17
	v_exp_f32_e32 v17, v84
	v_exp_f32_e32 v16, v85
	v_exp_f32_e32 v85, v86
	v_exp_f32_e32 v84, v87
	v_exp_f32_e32 v2, v82
	v_exp_f32_e32 v215, v83
	v_exp_f32_e32 v217, v66
	v_exp_f32_e32 v219, v67
	v_exp_f32_e32 v218, v68
	v_exp_f32_e32 v220, v69
	v_exp_f32_e32 v83, v70
	v_exp_f32_e32 v82, v71
	v_cvt_pk_bf16_f32 v66, v2, v215
	v_cvt_pk_bf16_f32 v67, v217, v219
	v_cvt_pk_bf16_f32 v68, v17, v16
	v_cvt_pk_bf16_f32 v69, v85, v84
	v_exp_f32_e32 v87, v88
	v_exp_f32_e32 v86, v89
	v_mfma_f32_32x32x16_bf16 v[34:49], v[174:177], v[66:69], v[34:49]
	v_exp_f32_e32 v89, v90
	v_exp_f32_e32 v88, v91
	v_exp_f32_e32 v91, v92
	v_exp_f32_e32 v90, v93
	v_exp_f32_e32 v93, v94
	v_exp_f32_e32 v92, v95
	v_exp_f32_e32 v97, v72
	v_exp_f32_e32 v96, v73
	v_exp_f32_e32 v195, v74
	v_exp_f32_e32 v194, v75
	v_cvt_pk_bf16_f32 v70, v87, v86
	v_cvt_pk_bf16_f32 v71, v89, v88
	v_cvt_pk_bf16_f32 v72, v91, v90
	v_cvt_pk_bf16_f32 v73, v93, v92
	v_mfma_f32_32x32x16_bf16 v[18:33], v[158:161], v[66:69], v[18:33]
	v_exp_f32_e32 v197, v76
	v_exp_f32_e32 v196, v77
	v_exp_f32_e32 v211, v78
	v_exp_f32_e32 v210, v79
	v_cvt_pk_bf16_f32 v74, v214, v216
	v_mfma_f32_32x32x16_bf16 v[34:49], v[170:173], v[70:73], v[34:49]
	v_cvt_pk_bf16_f32 v75, v218, v220
	v_cvt_pk_bf16_f32 v76, v83, v82
	v_cvt_pk_bf16_f32 v77, v97, v96
	v_exp_f32_e32 v213, v80
	v_exp_f32_e32 v212, v81
	v_mfma_f32_32x32x16_bf16 v[18:33], v[12:15], v[70:73], v[18:33]
	v_cvt_pk_bf16_f32 v78, v195, v194
	v_cvt_pk_bf16_f32 v79, v197, v196
	v_add_f32_e32 v2, v214, v2
	v_cvt_pk_bf16_f32 v80, v211, v210
	v_cvt_pk_bf16_f32 v81, v213, v212
	v_mfma_f32_32x32x16_bf16 v[34:49], v[166:169], v[74:77], v[34:49]
	v_add_f32_e32 v94, v216, v215
	v_add_f32_e32 v95, v218, v217
	v_add_f32_e32 v2, v94, v2
	v_add_f32_e32 v2, v95, v2
	v_pk_add_f32 v[16:17], v[82:83], v[16:17]
	v_pk_add_f32 v[66:67], v[96:97], v[84:85]
	v_mfma_f32_32x32x16_bf16 v[18:33], v[8:11], v[74:77], v[18:33]
	v_add_f32_e64 v68, v194, v86
	v_add_f32_e64 v69, v195, v87
	v_add_f32_e64 v82, v196, v88
	v_add_f32_e64 v83, v197, v89
	v_add_f32_e64 v84, v210, v90
	v_add_f32_e64 v85, v211, v91
	s_add_i32 s10, s60, 1
	v_pk_add_f32 v[86:87], v[212:213], v[92:93]
	s_and_b32 s60, s10, 3
	s_waitcnt vmcnt(6) lgkmcnt(0)
	v_mfma_f32_32x32x16_bf16 v[34:49], v[162:165], v[78:81], v[34:49]
	v_add_f32_e32 v162, v220, v219
	v_add_f32_e32 v2, v162, v2
	v_add_f32_e32 v2, v17, v2
	v_add_f32_e32 v2, v16, v2
	v_add_f32_e32 v2, v67, v2
	v_add_f32_e32 v2, v66, v2
	v_add_f32_e32 v2, v69, v2
	v_add_f32_e32 v2, v68, v2
	v_mfma_f32_32x32x16_bf16 v[18:33], v[4:7], v[78:81], v[18:33]
	v_add_f32_e32 v2, v83, v2
	v_add_f32_e32 v2, v82, v2
	v_add_f32_e32 v2, v85, v2
	v_add_f32_e32 v2, v84, v2
	v_add_f32_e32 v2, v87, v2
	s_barrier
	s_add_i32 s10, s64, 1
	v_add_f32_e32 v2, v86, v2
	s_and_b32 s64, s10, 3
	s_add_i32 s35, s35, 1
	v_add_f32_e32 v191, v191, v2
	s_cmp_ge_i32 s35, s34
	v_add_u32_e32 v209, 64, v209
	s_cbranch_scc1 .LBB0_765
.LBB0_745:
	s_mul_i32 s10, s60, 0x5400
	s_add_i32 s26, s10, 0
	s_add_i32 s27, s26, s36
	s_add_i32 s28, s26, s59
	s_and_b64 s[10:11], s[12:13], exec
	s_cselect_b32 s10, s28, s37
	s_add_i32 s11, s26, s58
	s_mov_b32 s26, m0
	s_mov_b32 m0, s27
	s_nop 0
	global_load_lds_dwordx4 v200, s[16:17]
	s_mov_b32 m0, s10
	s_or_b64 exec, s[12:13], 1
	global_load_lds_dwordx4 v201, s[16:17]
	s_mov_b64 exec, -1
	s_mov_b32 m0, s11
	s_nop 0
	global_load_lds_dwordx4 v198, s[18:19]
	s_mov_b32 m0, s26
	s_andn2_b64 vcc, exec, s[20:21]
	s_cbranch_vccnz .LBB0_756
	s_add_i32 s57, s57, -1
	s_cmp_lg_u32 s57, 0
	s_cbranch_scc0 .Lmla_m_adv
	s_add_u32 s16, s16, 0x21000
	s_addc_u32 s17, s17, 0
	s_add_u32 s18, s18, 0x21000
	s_addc_u32 s19, s19, 0
	s_branch .LBB0_756
.Lmla_m_adv:
	s_add_i32 s26, s54, 1
	s_bitcmp0_b32 s54, 0
	v_readlane_b32 s21, v252, 25
	s_mul_i32 s20, s26, s78
	s_cselect_b32 s27, s21, s82
	s_add_i32 s27, s27, s20
	s_cmpk_lt_i32 s27, 0x800
	s_cselect_b64 s[20:21], -1, 0
	s_cmpk_gt_i32 s27, 0x7ff
	s_cbranch_scc1 .LBB0_751
	s_lshl_b32 s1, s27, 5
	s_and_b32 s1, s1, 0xf00
	s_bfe_u32 s0, s27, 0x40007
	s_sub_i32 s1, 0x1000, s1
	s_ashr_i32 s55, s1, 6
	s_mul_i32 s0, s0, 0x840000
	s_add_u32 s0, s62, s0
	s_addc_u32 s1, s63, 0
	s_lshl_b32 s14, s27, 8
	s_and_b32 s56, s14, 0x700
	s_add_u32 s14, s0, s56
	s_addc_u32 s15, s1, 0
	s_add_u32 s14, s14, 0x80
	s_addc_u32 s15, s15, 0
.LBB0_751:
	s_andn2_b64 vcc, exec, s[20:21]
	s_cbranch_vccnz .LBB0_755
	v_mov_b32_e32 v2, s56
	v_cndmask_b32_e64 v4, 0, v2, s[4:5]
	v_cndmask_b32_e64 v2, 0, v2, s[6:7]
	v_add_u32_e32 v200, v4, v1
	v_add_u32_e32 v201, v2, v181
	s_mov_b64 s[20:21], -1
	s_mov_b32 s54, s26
	s_mov_b64 s[16:17], s[0:1]
	s_mov_b64 s[18:19], s[14:15]
	s_mov_b32 s57, s55
	s_branch .LBB0_756
.LBB0_755:
	s_mov_b64 s[20:21], 0
	s_mov_b32 s57, 0
.LBB0_756:
	s_mul_i32 s26, s64, 0x5400
	v_add_u32_e32 v2, s26, v205
	s_waitcnt lgkmcnt(3)
	ds_read_b128 v[4:7], v2 offset:6656
	s_waitcnt lgkmcnt(1)
	ds_read_b128 v[8:11], v2
	ds_read_b128 v[12:15], v2 offset:32
	ds_read_b128 v[158:161], v2 offset:6688
	ds_read_b128 v[162:165], v2 offset:64
	ds_read_b128 v[166:169], v2 offset:6720
	ds_read_b128 v[170:173], v2 offset:96
	ds_read_b128 v[174:177], v2 offset:6752
	ds_read_b128 v[194:197], v2 offset:128
	ds_read_b128 v[210:213], v2 offset:6784
	ds_read_b128 v[214:217], v2 offset:160
	ds_read_b128 v[218:221], v2 offset:6816
	v_subrev_u32_e32 v2, 59, v209
	s_waitcnt lgkmcnt(10)
	v_mfma_f32_32x32x16_bf16 v[82:97], v[8:11], v[134:137], v[50:65]
	v_mfma_f32_32x32x16_bf16 v[66:81], v[4:7], v[134:137], v[50:65]
	v_add_u32_e32 v6, s26, v206
	s_waitcnt lgkmcnt(9)
	v_mfma_f32_32x32x16_bf16 v[82:97], v[12:15], v[138:141], v[82:97]
	s_waitcnt lgkmcnt(8)
	v_mfma_f32_32x32x16_bf16 v[66:81], v[158:161], v[138:141], v[66:81]
	s_waitcnt lgkmcnt(7)
	v_mfma_f32_32x32x16_bf16 v[82:97], v[162:165], v[142:145], v[82:97]
	s_waitcnt lgkmcnt(6)
	v_mfma_f32_32x32x16_bf16 v[66:81], v[166:169], v[142:145], v[66:81]
	s_waitcnt lgkmcnt(5)
	v_mfma_f32_32x32x16_bf16 v[82:97], v[170:173], v[146:149], v[82:97]
	s_waitcnt lgkmcnt(4)
	v_mfma_f32_32x32x16_bf16 v[66:81], v[174:177], v[146:149], v[66:81]
	ds_read_b64_tr_b16 v[174:175], v6 offset:13312
	ds_read_b64_tr_b16 v[176:177], v6 offset:13824
	ds_read_b64_tr_b16 v[170:171], v6 offset:14336
	ds_read_b64_tr_b16 v[172:173], v6 offset:14848
	ds_read_b64_tr_b16 v[166:167], v6 offset:15360
	ds_read_b64_tr_b16 v[168:169], v6 offset:15872
	ds_read_b64_tr_b16 v[162:163], v6 offset:16384
	ds_read_b64_tr_b16 v[164:165], v6 offset:16896
	ds_read_b64_tr_b16 v[158:159], v6 offset:17408
	ds_read_b64_tr_b16 v[160:161], v6 offset:17920
	ds_read_b64_tr_b16 v[12:13], v6 offset:18432
	ds_read_b64_tr_b16 v[14:15], v6 offset:18944
	ds_read_b64_tr_b16 v[8:9], v6 offset:19456
	ds_read_b64_tr_b16 v[10:11], v6 offset:19968
	ds_read_b64_tr_b16 v[4:5], v6 offset:20480
	ds_read_b64_tr_b16 v[6:7], v6 offset:20992
	s_waitcnt lgkmcnt(14)
	v_mfma_f32_32x32x16_bf16 v[82:97], v[194:197], v[150:153], v[82:97]
	v_mfma_f32_32x32x16_bf16 v[66:81], v[210:213], v[150:153], v[66:81]
	v_mfma_f32_32x32x16_bf16 v[82:97], v[214:217], v[154:157], v[82:97]
	v_mfma_f32_32x32x16_bf16 v[66:81], v[218:221], v[154:157], v[66:81]
	v_subrev_u32_e32 v16, 27, v209
	v_cmp_le_i32_e32 vcc, v16, v208
	s_cmp_lg_u32 s35, -1
	s_nop 8
	v_cndmask_b32_e32 v16, v243, v66, vcc
	v_cmp_lt_i32_e32 vcc, v2, v208
	s_nop 1
	v_cndmask_b32_e32 v83, v243, v83, vcc
	v_cmp_le_i32_e32 vcc, v2, v208
	v_subrev_u32_e32 v2, 26, v209
	s_nop 0
	v_cndmask_b32_e32 v82, v243, v82, vcc
	v_cmp_le_i32_e32 vcc, v2, v208
	v_subrev_u32_e32 v2, 57, v209
	s_nop 0
	v_cndmask_b32_e32 v17, v243, v67, vcc
	v_cmp_le_i32_e32 vcc, v2, v208
	v_subrev_u32_e32 v2, 25, v209
	s_nop 0
	v_cndmask_b32_e32 v66, v243, v84, vcc
	v_cmp_le_i32_e32 vcc, v2, v208
	v_subrev_u32_e32 v2, 56, v209
	s_nop 0
	v_cndmask_b32_e32 v68, v243, v68, vcc
	v_cmp_le_i32_e32 vcc, v2, v208
	v_subrev_u32_e32 v2, 24, v209
	s_nop 0
	v_cndmask_b32_e32 v67, v243, v85, vcc
	v_cmp_le_i32_e32 vcc, v2, v208
	v_subrev_u32_e32 v2, 51, v209
	s_nop 0
	v_cndmask_b32_e32 v69, v243, v69, vcc
	v_cmp_le_i32_e32 vcc, v2, v208
	v_subrev_u32_e32 v2, 19, v209
	s_nop 0
	v_cndmask_b32_e32 v84, v243, v86, vcc
	v_cmp_le_i32_e32 vcc, v2, v208
	v_subrev_u32_e32 v2, 50, v209
	s_nop 0
	v_cndmask_b32_e32 v70, v243, v70, vcc
	v_cmp_le_i32_e32 vcc, v2, v208
	v_subrev_u32_e32 v2, 18, v209
	s_nop 0
	v_cndmask_b32_e32 v85, v243, v87, vcc
	v_cmp_le_i32_e32 vcc, v2, v208
	v_subrev_u32_e32 v2, 49, v209
	s_nop 0
	v_cndmask_b32_e32 v71, v243, v71, vcc
	v_cmp_le_i32_e32 vcc, v2, v208
	v_subrev_u32_e32 v2, 17, v209
	s_nop 0
	v_cndmask_b32_e32 v86, v243, v88, vcc
	v_cmp_le_i32_e32 vcc, v2, v208
	v_subrev_u32_e32 v2, 48, v209
	s_nop 0
	v_cndmask_b32_e32 v72, v243, v72, vcc
	v_cmp_le_i32_e32 vcc, v2, v208
	v_add_u32_e32 v2, -16, v209
	s_nop 0
	v_cndmask_b32_e32 v87, v243, v89, vcc
	v_cmp_le_i32_e32 vcc, v2, v208
	v_subrev_u32_e32 v2, 43, v209
	s_nop 0
	v_cndmask_b32_e32 v73, v243, v73, vcc
	v_cmp_le_i32_e32 vcc, v2, v208
	v_add_u32_e32 v2, -11, v209
	s_nop 0
	v_cndmask_b32_e32 v88, v243, v90, vcc
	v_cmp_le_i32_e32 vcc, v2, v208
	v_subrev_u32_e32 v2, 42, v209
	s_nop 0
	v_cndmask_b32_e32 v74, v243, v74, vcc
	v_cmp_le_i32_e32 vcc, v2, v208
	v_add_u32_e32 v2, -10, v209
	s_nop 0
	v_cndmask_b32_e32 v89, v243, v91, vcc
	v_cmp_le_i32_e32 vcc, v2, v208
	v_subrev_u32_e32 v2, 41, v209
	s_nop 0
	v_cndmask_b32_e32 v75, v243, v75, vcc
	v_cmp_le_i32_e32 vcc, v2, v208
	v_add_u32_e32 v2, -9, v209
	s_nop 0
	v_cndmask_b32_e32 v90, v243, v92, vcc
	v_cmp_le_i32_e32 vcc, v2, v208
	v_subrev_u32_e32 v2, 40, v209
	s_nop 0
	v_cndmask_b32_e32 v76, v243, v76, vcc
	v_cmp_le_i32_e32 vcc, v2, v208
	v_add_u32_e32 v2, -8, v209
	s_nop 0
	v_cndmask_b32_e32 v91, v243, v93, vcc
	v_cmp_le_i32_e32 vcc, v2, v208
	v_subrev_u32_e32 v2, 35, v209
	s_nop 0
	v_cndmask_b32_e32 v77, v243, v77, vcc
	v_cmp_le_i32_e32 vcc, v2, v208
	v_add_u32_e32 v2, -3, v209
	s_nop 0
	v_cndmask_b32_e32 v92, v243, v94, vcc
	v_cmp_le_i32_e32 vcc, v2, v208
	v_subrev_u32_e32 v2, 34, v209
	s_nop 0
	v_cndmask_b32_e32 v78, v243, v78, vcc
	v_cmp_le_i32_e32 vcc, v2, v208
	v_add_u32_e32 v2, -2, v209
	s_nop 0
	v_cndmask_b32_e32 v93, v243, v95, vcc
	v_cmp_le_i32_e32 vcc, v2, v208
	v_subrev_u32_e32 v2, 33, v209
	s_nop 0
	v_cndmask_b32_e32 v79, v243, v79, vcc
	v_cmp_le_i32_e32 vcc, v2, v208
	v_add_u32_e32 v2, -1, v209
	s_nop 0
	v_cndmask_b32_e32 v94, v243, v96, vcc
	v_cmp_le_i32_e32 vcc, v2, v208
	v_subrev_u32_e32 v2, 32, v209
	v_max3_f32 v96, v16, v17, v68
	v_cndmask_b32_e32 v80, v243, v80, vcc
	v_cmp_le_i32_e32 vcc, v2, v208
	v_max3_f32 v2, v82, v83, v66
	v_max3_f32 v2, v2, v67, v84
	v_max3_f32 v96, v96, v69, v70
	v_max3_f32 v2, v2, v85, v86
	v_max3_f32 v96, v96, v71, v72
	v_cndmask_b32_e32 v95, v243, v97, vcc
	v_cmp_le_i32_e32 vcc, v209, v208
	v_max3_f32 v2, v2, v87, v88
	v_max3_f32 v96, v96, v73, v74
	v_cndmask_b32_e32 v81, v243, v81, vcc
	v_max3_f32 v2, v2, v89, v90
	v_max3_f32 v96, v96, v75, v76
	v_max3_f32 v2, v2, v91, v92
	v_max3_f32 v96, v96, v77, v78
	v_max3_f32 v2, v2, v93, v94
	v_max3_f32 v96, v96, v79, v80
	v_max_f32_e32 v97, v95, v81
	v_max3_f32 v2, v2, v96, v97
	ds_bpermute_b32 v96, v223, v2
	s_waitcnt lgkmcnt(0)
	v_max_f32_e32 v96, v2, v96
	s_cbranch_scc0 .Lmla_m_first
	v_cmp_lt_f32_e32 vcc, s81, v96
	s_cbranch_vccz .LBB0_744
	v_max_f32_e32 v2, v96, v96
	v_max_f32_e32 v2, 0, v2
	s_branch .Lmla_m_resc
.Lmla_m_first:
	v_mov_b32_e32 v2, v96
.Lmla_m_resc:
	v_exp_f32_e64 v52, -v2
	v_add_f32_e32 v193, v193, v2
	v_xor_b32_e32 v50, 0x80000000, v193
	v_pk_add_f32 v[82:83], v[82:83], v[2:3] op_sel_hi:[1,0] neg_lo:[0,1] neg_hi:[0,1]
	v_pk_add_f32 v[16:17], v[16:17], v[2:3] op_sel_hi:[1,0] neg_lo:[0,1] neg_hi:[0,1]
	v_pk_add_f32 v[66:67], v[66:67], v[2:3] op_sel_hi:[1,0] neg_lo:[0,1] neg_hi:[0,1]
	v_pk_add_f32 v[68:69], v[68:69], v[2:3] op_sel_hi:[1,0] neg_lo:[0,1] neg_hi:[0,1]
	v_pk_add_f32 v[84:85], v[84:85], v[2:3] op_sel_hi:[1,0] neg_lo:[0,1] neg_hi:[0,1]
	v_pk_add_f32 v[70:71], v[70:71], v[2:3] op_sel_hi:[1,0] neg_lo:[0,1] neg_hi:[0,1]
	v_pk_add_f32 v[86:87], v[86:87], v[2:3] op_sel_hi:[1,0] neg_lo:[0,1] neg_hi:[0,1]
	v_pk_add_f32 v[72:73], v[72:73], v[2:3] op_sel_hi:[1,0] neg_lo:[0,1] neg_hi:[0,1]
	v_pk_add_f32 v[88:89], v[88:89], v[2:3] op_sel_hi:[1,0] neg_lo:[0,1] neg_hi:[0,1]
	v_pk_add_f32 v[74:75], v[74:75], v[2:3] op_sel_hi:[1,0] neg_lo:[0,1] neg_hi:[0,1]
	v_pk_add_f32 v[90:91], v[90:91], v[2:3] op_sel_hi:[1,0] neg_lo:[0,1] neg_hi:[0,1]
	v_pk_add_f32 v[76:77], v[76:77], v[2:3] op_sel_hi:[1,0] neg_lo:[0,1] neg_hi:[0,1]
	v_pk_add_f32 v[92:93], v[92:93], v[2:3] op_sel_hi:[1,0] neg_lo:[0,1] neg_hi:[0,1]
	v_pk_add_f32 v[78:79], v[78:79], v[2:3] op_sel_hi:[1,0] neg_lo:[0,1] neg_hi:[0,1]
	v_pk_add_f32 v[94:95], v[94:95], v[2:3] op_sel_hi:[1,0] neg_lo:[0,1] neg_hi:[0,1]
	v_pk_add_f32 v[80:81], v[80:81], v[2:3] op_sel_hi:[1,0] neg_lo:[0,1] neg_hi:[0,1]
	v_pk_mul_f32 v[48:49], v[48:49], v[52:53] op_sel_hi:[1,0]
	v_pk_mul_f32 v[46:47], v[46:47], v[52:53] op_sel_hi:[1,0]
	v_pk_mul_f32 v[44:45], v[44:45], v[52:53] op_sel_hi:[1,0]
	v_pk_mul_f32 v[42:43], v[42:43], v[52:53] op_sel_hi:[1,0]
	v_pk_mul_f32 v[40:41], v[40:41], v[52:53] op_sel_hi:[1,0]
	v_pk_mul_f32 v[38:39], v[38:39], v[52:53] op_sel_hi:[1,0]
	v_pk_mul_f32 v[36:37], v[36:37], v[52:53] op_sel_hi:[1,0]
	v_pk_mul_f32 v[34:35], v[34:35], v[52:53] op_sel_hi:[1,0]
	v_pk_mul_f32 v[32:33], v[32:33], v[52:53] op_sel_hi:[1,0]
	v_pk_mul_f32 v[30:31], v[30:31], v[52:53] op_sel_hi:[1,0]
	v_pk_mul_f32 v[28:29], v[28:29], v[52:53] op_sel_hi:[1,0]
	v_pk_mul_f32 v[26:27], v[26:27], v[52:53] op_sel_hi:[1,0]
	v_pk_mul_f32 v[24:25], v[24:25], v[52:53] op_sel_hi:[1,0]
	v_pk_mul_f32 v[22:23], v[22:23], v[52:53] op_sel_hi:[1,0]
	v_pk_mul_f32 v[20:21], v[20:21], v[52:53] op_sel_hi:[1,0]
	v_pk_mul_f32 v[18:19], v[18:19], v[52:53] op_sel_hi:[1,0]
	v_mul_f32_e32 v191, v191, v52
	v_mov_b32_e32 v51, v50
	v_mov_b32_e32 v52, v50
	v_mov_b32_e32 v53, v50
	v_mov_b32_e32 v54, v50
	v_mov_b32_e32 v55, v50
	v_mov_b32_e32 v56, v50
	v_mov_b32_e32 v57, v50
	v_mov_b32_e32 v58, v50
	v_mov_b32_e32 v59, v50
	v_mov_b32_e32 v60, v50
	v_mov_b32_e32 v61, v50
	v_mov_b32_e32 v62, v50
	v_mov_b32_e32 v63, v50
	v_mov_b32_e32 v64, v50
	v_mov_b32_e32 v65, v50
	s_branch .LBB0_744
